# scan LDS operand buffers: row strides 272/144 -> 288/160 bytes so the MFMA fragment ds_read_b128 groups are bank-conflict free; small arrays moved up 0x2800
# speedup vs baseline: 1.0645x; 1.0129x over previous
; #define LAS __attribute__((address_space(3)))
; #define SC_BAR() do { asm volatile("s_waitcnt lgkmcnt(0)" ::: "memory"); __builtin_amdgcn_s_barrier(); asm volatile("" ::: "memory"); } while (0)
; __device__ __forceinline__ void gdn_scan(const Params& P, LAS unsigned char* lds, int sb, int tid, int lane, int wave) {
;     ...
;     const int bh = sb & 7, part = sb >> 3;
;     const int b = bh >> 2, h = bh & 3, col = lane & 15, g = lane >> 4;
;     const int item0 = bh * 128;
;     if (tid == 0) *(volatile LAS unsigned*)(lds + SC_RDY) = 0u;
;     SC_BAR();
;     if (wave >= 4) {
.LBB0_2068:
	s_and_b64 vcc, exec, s[0:1]
	s_cbranch_vccz .LBB0_2205
	s_mov_b64 s[0:1], exec
	v_readlane_b32 s6, v255, 2
	v_readlane_b32 s7, v255, 3
	s_and_b64 s[6:7], s[0:1], s[6:7]
	s_mov_b64 exec, s[6:7]
	s_add_i32 s3, 0, 0x27a00
	v_mov_b32_e32 v1, 0
	v_mov_b32_e32 v2, s3
	ds_write_b32 v2, v1
	s_or_b64 exec, exec, s[0:1]
	s_waitcnt lgkmcnt(0)
	s_barrier
	s_ashr_i32 s0, s2, 3
	s_cmpk_lt_u32 s74, 0x100
	s_mov_b64 s[6:7], -1
	s_cbranch_scc0 .LBB0_2154
	v_readlane_b32 s8, v254, 56
	v_readlane_b32 s9, v254, 57
	s_mov_b64 s[10:11], -1
	s_mov_b64 s[6:7], 0
	s_cmp_lt_i32 s8, 3
	s_mov_b64 s[8:9], 0
	s_cbranch_scc0 .LBB0_2076
	s_and_b64 vcc, exec, s[10:11]
	s_cbranch_vccnz .LBB0_2143

; __device__ __forceinline__ void gdn_scan(const Params& P, LAS unsigned char* lds, int sb, int tid, int lane, int wave) {
;     ...
;     if (wave == 3) {
;         const unsigned* flags = (const unsigned*)(ws + WS_CTL) + CW_GFLAG + item0;
;         unsigned rdy = 0;
;     ...
;         { unsigned sp = 0; while (rdy < 4u && ++sp < (1u << 22)) { SC_POLLSTEP(); if (rdy < 4u) __builtin_amdgcn_s_sleep(16); } }
.LBB0_2076:
	v_readlane_b32 s8, v254, 56
	v_readlane_b32 s9, v254, 57
	s_cmp_eq_u32 s8, 3
	s_mov_b64 s[8:9], -1
	s_cbranch_scc0 .LBB0_2142
	s_mov_b32 s1, 0
	s_mov_b32 s10, 0x3fffff
	v_mov_b32_e32 v3, 0
	s_add_i32 s3, 0, 0x27a00
	s_branch .LBB0_2080

; __device__ __forceinline__ void gdn_scan(const Params& P, LAS unsigned char* lds, int sb, int tid, int lane, int wave) {
;     ...
;         { unsigned sp = 0; while (rdy < 4u && ++sp < (1u << 22)) { SC_POLLSTEP(); if (rdy < 4u) __builtin_amdgcn_s_sleep(16); } }
.LBB0_2080:
	v_add_u32_e32 v2, s1, v182
	v_lshl_add_u64 v[4:5], v[2:3], 2, s[76:77]
	global_load_dword v1, v[4:5], off sc1
	s_waitcnt vmcnt(0)
	v_cmp_ne_u32_e32 vcc, 0, v1
	s_not_b64 s[8:9], vcc
	s_ff1_i32_b64 s8, s[8:9]
	s_min_u32 s11, s8, 64
	v_cmp_gt_u32_e32 vcc, s11, v182
	s_and_saveexec_b64 s[8:9], vcc
	v_lshl_add_u32 v2, v2, 2, 0
	v_add_u32_e32 v2, 0x23000, v2
	ds_write_b32 v2, v1
	s_or_b64 exec, exec, s[8:9]
	s_waitcnt lgkmcnt(0)
	s_add_i32 s1, s1, s11
	s_and_saveexec_b64 s[8:9], s[4:5]
	v_mov_b32_e32 v1, s3
	v_mov_b32_e32 v2, s1
	ds_write_b32 v1, v2
	s_or_b64 exec, exec, s[8:9]
	s_cmp_gt_u32 s1, 3
	s_mov_b64 s[8:9], -1
	s_cbranch_scc1 .LBB0_2078
	v_add_u32_e32 v2, s1, v182
	v_lshl_add_u64 v[4:5], v[2:3], 2, s[76:77]
	s_sleep 16
	global_load_dword v1, v[4:5], off sc1
	s_waitcnt vmcnt(0)
	v_cmp_ne_u32_e32 vcc, 0, v1
	s_not_b64 s[8:9], vcc
	s_ff1_i32_b64 s8, s[8:9]
	s_min_u32 s11, s8, 64
	v_cmp_gt_u32_e32 vcc, s11, v182
	s_and_saveexec_b64 s[8:9], vcc
	v_lshl_add_u32 v2, v2, 2, 0
	v_add_u32_e32 v2, 0x23000, v2
	ds_write_b32 v2, v1
	s_or_b64 exec, exec, s[8:9]
	s_waitcnt lgkmcnt(0)
	s_add_i32 s1, s1, s11
	s_and_saveexec_b64 s[8:9], s[4:5]
	v_mov_b32_e32 v1, s3
	v_mov_b32_e32 v2, s1
	ds_write_b32 v1, v2
	s_or_b64 exec, exec, s[8:9]
	s_cmp_gt_u32 s1, 3
	s_mov_b64 s[8:9], -1
	s_cbranch_scc1 .LBB0_2078
	v_add_u32_e32 v2, s1, v182
	v_lshl_add_u64 v[4:5], v[2:3], 2, s[76:77]
	s_sleep 16
	global_load_dword v1, v[4:5], off sc1
	s_waitcnt vmcnt(0)
	v_cmp_ne_u32_e32 vcc, 0, v1
	s_not_b64 s[8:9], vcc
	s_ff1_i32_b64 s8, s[8:9]
	s_min_u32 s11, s8, 64
	v_cmp_gt_u32_e32 vcc, s11, v182
	s_and_saveexec_b64 s[8:9], vcc
	v_lshl_add_u32 v2, v2, 2, 0
	v_add_u32_e32 v2, 0x23000, v2
	ds_write_b32 v2, v1
	s_or_b64 exec, exec, s[8:9]
	s_waitcnt lgkmcnt(0)
	s_add_i32 s1, s1, s11
	s_and_saveexec_b64 s[8:9], s[4:5]
	s_cbranch_execnz .LBB0_2094
	s_or_b64 exec, exec, s[8:9]
	s_cmp_gt_u32 s1, 3
	s_mov_b64 s[8:9], -1
	s_cbranch_scc1 .LBB0_2079
	s_branch .LBB0_2095

; #define SC_BAR() do { asm volatile("s_waitcnt lgkmcnt(0)" ::: "memory"); __builtin_amdgcn_s_barrier(); asm volatile("" ::: "memory"); } while (0)
; __device__ __forceinline__ void gdn_scan(const Params& P, LAS unsigned char* lds, int sb, int tid, int lane, int wave) {
;     ...
;         SC_BAR();
; #pragma unroll 1
;         for (int n2 = 0; n2 < NCH; ++n2) {
;             { const unsigned need = (unsigned)(n2 + 1 + 3) < 128u ? (unsigned)(n2 + 1 + 3) : 127u; unsigned sp = 0;
;               while (rdy <= need && rdy < 128u && ++sp < (1u << 22)) { SC_POLLSTEP(); if (rdy <= need) __builtin_amdgcn_s_sleep(8); } }
.LBB0_2105:
	s_waitcnt lgkmcnt(0)
	s_barrier
	s_mov_b32 s3, 0
	s_movk_i32 s10, 0x80
	v_mov_b32_e32 v3, 0
	s_add_i32 s11, 0, 0x27a00
	s_branch .LBB0_2108

; #define SC_BAR() do { asm volatile("s_waitcnt lgkmcnt(0)" ::: "memory"); __builtin_amdgcn_s_barrier(); asm volatile("" ::: "memory"); } while (0)
; __device__ __forceinline__ void gdn_scan(const Params& P, LAS unsigned char* lds, int sb, int tid, int lane, int wave) {
;     ...
;         { unsigned sp = 0; while (rdy < 4u && ++sp < (1u << 22)) { SC_POLLSTEP(); if (rdy < 4u) __builtin_amdgcn_s_sleep(16); } }
;         SC_BAR();
; #pragma unroll 1
;         for (int n2 = 0; n2 < NCH; ++n2) {
;             { const unsigned need = (unsigned)(n2 + 1 + 3) < 128u ? (unsigned)(n2 + 1 + 3) : 127u; unsigned sp = 0;
;               while (rdy <= need && rdy < 128u && ++sp < (1u << 22)) { SC_POLLSTEP(); if (rdy <= need) __builtin_amdgcn_s_sleep(8); } }
.LBB0_2114:
	s_or_b64 exec, exec, s[8:9]
	s_waitcnt vmcnt(0)
	v_cmp_ne_u32_e32 vcc, 0, v1
	s_not_b64 s[8:9], vcc
	s_ff1_i32_b64 s8, s[8:9]
	s_min_u32 s14, s8, 64
	v_cmp_gt_u32_e32 vcc, s14, v182
	s_and_saveexec_b64 s[8:9], vcc
	v_lshl_add_u32 v2, v2, 2, 0
	v_add_u32_e32 v2, 0x23000, v2
	ds_write_b32 v2, v1
	s_or_b64 exec, exec, s[8:9]
	s_waitcnt lgkmcnt(0)
	s_add_i32 s1, s1, s14
	s_and_saveexec_b64 s[8:9], s[4:5]
	v_mov_b32_e32 v1, s11
	v_mov_b32_e32 v2, s1
	ds_write_b32 v1, v2
	s_or_b64 exec, exec, s[8:9]
	s_cmp_gt_u32 s1, s12
	s_mov_b64 s[8:9], -1
	s_cbranch_scc1 .LBB0_2110
	v_add_u32_e32 v2, s1, v182
	v_cmp_gt_u32_e32 vcc, s10, v2
	v_mov_b32_e32 v1, 0
	s_sleep 8
	s_and_saveexec_b64 s[8:9], vcc
	s_cbranch_execz .LBB0_2121
	v_lshl_add_u64 v[4:5], v[2:3], 2, s[76:77]
	global_load_dword v1, v[4:5], off sc1

; #define SC_BAR() do { asm volatile("s_waitcnt lgkmcnt(0)" ::: "memory"); __builtin_amdgcn_s_barrier(); asm volatile("" ::: "memory"); } while (0)
; __device__ __forceinline__ void gdn_scan(const Params& P, LAS unsigned char* lds, int sb, int tid, int lane, int wave) {
;     ...
;         { unsigned sp = 0; while (rdy < 4u && ++sp < (1u << 22)) { SC_POLLSTEP(); if (rdy < 4u) __builtin_amdgcn_s_sleep(16); } }
;         SC_BAR();
; #pragma unroll 1
;         for (int n2 = 0; n2 < NCH; ++n2) {
;             { const unsigned need = (unsigned)(n2 + 1 + 3) < 128u ? (unsigned)(n2 + 1 + 3) : 127u; unsigned sp = 0;
;               while (rdy <= need && rdy < 128u && ++sp < (1u << 22)) { SC_POLLSTEP(); if (rdy <= need) __builtin_amdgcn_s_sleep(8); } }
.LBB0_2128:
	s_or_b64 exec, exec, s[8:9]
	s_waitcnt vmcnt(0)
	v_cmp_ne_u32_e32 vcc, 0, v1
	s_not_b64 s[8:9], vcc
	s_ff1_i32_b64 s8, s[8:9]
	s_min_u32 s14, s8, 64
	v_cmp_gt_u32_e32 vcc, s14, v182
	s_and_saveexec_b64 s[8:9], vcc
	v_lshl_add_u32 v2, v2, 2, 0
	v_add_u32_e32 v2, 0x23000, v2
	ds_write_b32 v2, v1
	s_or_b64 exec, exec, s[8:9]
	s_waitcnt lgkmcnt(0)
	s_add_i32 s1, s1, s14
	s_and_saveexec_b64 s[8:9], s[4:5]
	s_cbranch_execnz .LBB0_2132
	s_or_b64 exec, exec, s[8:9]
	s_cmp_gt_u32 s1, s12
	s_mov_b64 s[8:9], -1
	s_cbranch_scc1 .LBB0_2111
	s_branch .LBB0_2133

; #define SC_BAR() do { asm volatile("s_waitcnt lgkmcnt(0)" ::: "memory"); __builtin_amdgcn_s_barrier(); asm volatile("" ::: "memory"); } while (0)
; __device__ __forceinline__ void gdn_scan(const Params& P, LAS unsigned char* lds, int sb, int tid, int lane, int wave) {
;     ...
;         { unsigned sp = 0; while (rdy < 4u && ++sp < (1u << 22)) { SC_POLLSTEP(); if (rdy < 4u) __builtin_amdgcn_s_sleep(16); } }
;         SC_BAR();
; #pragma unroll 1
;         for (int n2 = 0; n2 < NCH; ++n2) {
;             { const unsigned need = (unsigned)(n2 + 1 + 3) < 128u ? (unsigned)(n2 + 1 + 3) : 127u; unsigned sp = 0;
;               while (rdy <= need && rdy < 128u && ++sp < (1u << 22)) { SC_POLLSTEP(); if (rdy <= need) __builtin_amdgcn_s_sleep(8); } }
;             if (rdy < 128u && rdy < (unsigned)(n2 & 127) + 16u) SC_POLLSTEP();
;             SC_BAR();
.LBB0_2137:
	s_or_b64 exec, exec, s[8:9]
	s_waitcnt vmcnt(0)
	v_cmp_ne_u32_e32 vcc, 0, v1
	s_not_b64 s[8:9], vcc
	s_ff1_i32_b64 s8, s[8:9]
	s_min_u32 s12, s8, 64
	v_cmp_gt_u32_e32 vcc, s12, v182
	s_and_saveexec_b64 s[8:9], vcc
	v_lshl_add_u32 v2, v2, 2, 0
	v_add_u32_e32 v2, 0x23000, v2
	ds_write_b32 v2, v1
	s_or_b64 exec, exec, s[8:9]
	s_waitcnt lgkmcnt(0)
	s_add_i32 s1, s1, s12
	s_and_saveexec_b64 s[8:9], s[4:5]
	s_cbranch_execz .LBB0_2106
	v_mov_b32_e32 v1, s11
	v_mov_b32_e32 v2, s1
	ds_write_b32 v1, v2
	s_branch .LBB0_2106

; __device__ __forceinline__ void gdn_scan(const Params& P, LAS unsigned char* lds, int sb, int tid, int lane, int wave) {
;     ...
;     f32x4 S[8];
; #pragma unroll
;     for (int i = 0; i < 8; ++i) S[i] = (f32x4){0.f, 0.f, 0.f, 0.f};
;     SC_BAR();
; #pragma unroll 1
;     for (int n2 = 0; n2 < NCH; ++n2) {
;         if (SCAN_REPS > 1 && (n2 & 127) == 0) {
; #pragma unroll
;             for (int i = 0; i < 8; ++i) S[i] = (f32x4){0.f, 0.f, 0.f, 0.f};
;         }
;         if (SCAN_EXP == 2 && n2 < 128) { SC_BAR(); continue; }
;         const int par = n2 & 1;
;         LAS unsigned char* buf = lds + par * SC_BUF;
;         bf16x8 fA[16], fB[16], fC[16], fD[8];
; #pragma unroll
;         for (int rho = 0; rho < 4; ++rho)
; #pragma unroll
;             for (int s = 0; s < 4; ++s) fA[rho * 4 + s] = *(const LAS bf16x8*)(buf + SC_WN + (16 * rho + col) * 272 + (32 * s + 8 * g) * 2);
; #pragma unroll
;         for (int rho = 0; rho < 4; ++rho)
; #pragma unroll
;             for (int s = 0; s < 4; ++s) fB[rho * 4 + s] = *(const LAS bf16x8*)(buf + SC_QD + (16 * rho + col) * 272 + (32 * s + 8 * g) * 2);
;         const LAS v4u* ufp = (const LAS v4u*)(lds + SC_UFS + par * (SCAN_NWC * 2048) + wave * 2048 + lane * 32);
;         const v4u uf0 = ufp[0], uf1 = ufp[1];
;         const float dec = ((const LAS float*)(lds + SC_DECS))[n2 & 127];
;         bf16x8 Bs[4];
; #pragma unroll
;         for (int s = 0; s < 4; ++s) Bs[s] = pack_b(S[2 * s], S[2 * s + 1]);
;         f32x4 Vn[4], Oc[4];
;         Vn[0] = (f32x4){bflo(uf0.x), bfhi(uf0.x), bflo(uf0.y), bfhi(uf0.y)}; Vn[1] = (f32x4){bflo(uf0.z), bfhi(uf0.z), bflo(uf0.w), bfhi(uf0.w)};
;         Vn[2] = (f32x4){bflo(uf1.x), bfhi(uf1.x), bflo(uf1.y), bfhi(uf1.y)}; Vn[3] = (f32x4){bflo(uf1.z), bfhi(uf1.z), bflo(uf1.w), bfhi(uf1.w)};
;         __builtin_amdgcn_sched_barrier(0);
;         PIN16(fA);
; #pragma unroll
;         for (int s = 0; s < 4; ++s)
; #pragma unroll
;             for (int rho = 0; rho < 4; ++rho) Vn[rho] = __builtin_amdgcn_mfma_f32_16x16x32_bf16(fA[rho * 4 + s], Bs[s], Vn[rho], 0, 0, 0);
;         __builtin_amdgcn_sched_barrier(0);
; #pragma unroll
;         for (int tau = 0; tau < 8; ++tau)
; #pragma unroll
;             for (int s = 0; s < 2; ++s) fC[tau * 2 + s] = *(const LAS bf16x8*)(buf + SC_KD + (16 * tau + col) * 144 + (32 * s + 8 * g) * 2);
;         __builtin_amdgcn_sched_barrier(0);
;         PIN16(fB);
.LBB0_2144:
	v_readlane_b32 s4, v254, 56
	s_lshl_b32 s3, s4, 11
	s_add_i32 s3, s3, 0
	v_lshrrev_b32_e32 v2, 2, v182
	s_add_i32 s3, s3, 0x21000
	v_and_b32_e32 v3, 12, v2
	v_lshl_add_u32 v1, v182, 5, s3
	s_and_b32 s3, s74, 0xc0
	v_mul_u32_u24_e32 v41, 0x90, v3
	v_or_b32_e32 v3, 3, v2
	s_add_i32 s3, s3, 0
	v_mul_u32_u24_e32 v42, 0x90, v3
	v_or_b32_e32 v3, 19, v2
	s_waitcnt lgkmcnt(0)
	s_barrier
	v_readlane_b32 s5, v254, 57
	s_add_i32 s3, s3, 0x23200
	v_or_b32_e32 v4, 0x70, v182
	v_mul_u32_u24_e32 v43, 0x90, v3
	v_or_b32_e32 v3, 35, v2
	v_or_b32_e32 v2, 51, v2
	s_mov_b32 s1, 0
	v_lshl_add_u32 v35, v142, 2, s3
	v_mul_u32_u24_e32 v36, 0x120, v142
	v_mul_u32_u24_e32 v37, 0x120, v143
	v_mul_u32_u24_e32 v38, 0xa0, v142
	v_mul_u32_u24_e32 v39, 0xa0, v143
	v_mul_u32_u24_e32 v40, 0xa0, v4
	v_mul_u32_u24_e32 v44, 0x90, v3
	v_mul_u32_u24_e32 v45, 0x90, v2
	s_add_i32 s3, 0, 0x23000
	v_add_u32_e32 v46, 0, v141
	v_mov_b32_e32 v2, 0
	v_mov_b32_e32 v3, 0
	v_mov_b32_e32 v4, 0
	v_mov_b32_e32 v5, 0
	v_mov_b32_e32 v6, 0
	v_mov_b32_e32 v7, 0
	v_mov_b32_e32 v8, 0
	v_mov_b32_e32 v9, 0
	v_mov_b32_e32 v10, 0
	v_mov_b32_e32 v11, 0
	v_mov_b32_e32 v12, 0
	v_mov_b32_e32 v13, 0
	v_mov_b32_e32 v14, 0
	v_mov_b32_e32 v15, 0
	v_mov_b32_e32 v16, 0
	v_mov_b32_e32 v17, 0
	v_mov_b32_e32 v18, 0
	v_mov_b32_e32 v19, 0
	v_mov_b32_e32 v20, 0
	v_mov_b32_e32 v21, 0
	v_mov_b32_e32 v22, 0
	v_mov_b32_e32 v23, 0
	v_mov_b32_e32 v24, 0
	v_mov_b32_e32 v25, 0
	v_mov_b32_e32 v26, 0
	v_mov_b32_e32 v27, 0
	v_mov_b32_e32 v28, 0
	v_mov_b32_e32 v29, 0
	v_mov_b32_e32 v30, 0
	v_mov_b32_e32 v31, 0
	v_mov_b32_e32 v32, 0
	v_mov_b32_e32 v33, 0
	s_movk_i32 s4, 0x7fff
	s_mov_b32 s5, 0xffff0000
	v_mov_b32_e32 v212, 0
	v_mov_b32_e32 v213, 0
	v_mov_b32_e32 v214, 0
	v_mov_b32_e32 v215, 0
	v_mov_b32_e32 v216, 0
	v_mov_b32_e32 v217, 0
	v_mov_b32_e32 v218, 0
	v_mov_b32_e32 v219, 0
	v_mov_b32_e32 v220, 0
	v_mov_b32_e32 v221, 0
	v_mov_b32_e32 v222, 0
	v_mov_b32_e32 v223, 0
	v_mov_b32_e32 v224, 0
	v_mov_b32_e32 v225, 0
	v_mov_b32_e32 v226, 0
	v_mov_b32_e32 v227, 0
.LBB0_2145:
	s_and_b32 s6, s1, 1
	s_mul_i32 s7, s6, 0x10800
	v_add_u32_e32 v47, s7, v46
	v_lshl_add_u32 v34, s6, 12, v1
	v_add_u32_e32 v158, v47, v37
	ds_read_b128 v[48:51], v34
	ds_read_b128 v[52:55], v34 offset:16
	v_mov_b32_e32 v34, s3
	v_add_u32_e32 v141, v47, v36
	ds_read_b32 v34, v34
	ds_read_b128 v[80:83], v158 offset:192
	ds_read_b128 v[84:87], v158 offset:128
	ds_read_b128 v[88:91], v158 offset:64
	ds_read_b128 v[92:95], v158
	ds_read_b128 v[96:99], v141 offset:9408
	ds_read_b128 v[100:103], v141 offset:9344
	ds_read_b128 v[104:107], v141 offset:9280
	ds_read_b128 v[108:111], v141 offset:9216
	ds_read_b128 v[112:115], v141 offset:4800
	ds_read_b128 v[116:119], v141 offset:4736
	ds_read_b128 v[120:123], v141 offset:4672
	ds_read_b128 v[124:127], v141 offset:4608
	ds_read_b128 v[128:131], v141 offset:192
	ds_read_b128 v[132:135], v141 offset:128
	ds_read_b128 v[136:139], v141 offset:64
	ds_read_b128 v[142:145], v141
	ds_read_b128 v[146:149], v158 offset:18624
	ds_read_b128 v[150:153], v158 offset:18560
	ds_read_b128 v[154:157], v158 offset:18496
	ds_read_b128 v[158:161], v158 offset:18432
	ds_read_b128 v[162:165], v141 offset:27840
	ds_read_b128 v[166:169], v141 offset:27776
	ds_read_b128 v[170:173], v141 offset:27712
	ds_read_b128 v[174:177], v141 offset:27648
	ds_read_b128 v[178:181], v141 offset:23232
	ds_read_b128 v[184:187], v141 offset:23168
	ds_read_b128 v[188:191], v141 offset:23104
	ds_read_b128 v[192:195], v141 offset:23040
	ds_read_b128 v[196:199], v141 offset:18624
	ds_read_b128 v[200:203], v141 offset:18560
	ds_read_b128 v[204:207], v141 offset:18496
	ds_read_b128 v[208:211], v141 offset:18432
	s_waitcnt lgkmcnt(15)
	v_lshlrev_b32_e32 v72, 16, v48
	v_and_b32_e32 v73, 0xffff0000, v48
	v_lshlrev_b32_e32 v74, 16, v49
	v_and_b32_e32 v75, 0xffff0000, v49
	v_lshlrev_b32_e32 v48, 16, v50
	v_and_b32_e32 v49, 0xffff0000, v50
	v_lshlrev_b32_e32 v50, 16, v51
	v_and_b32_e32 v51, 0xffff0000, v51
	v_lshlrev_b32_e32 v76, 16, v52
	v_and_b32_e32 v77, 0xffff0000, v52
	v_lshlrev_b32_e32 v78, 16, v53
	v_and_b32_e32 v79, 0xffff0000, v53
	v_lshlrev_b32_e32 v52, 16, v54
	v_and_b32_e32 v53, 0xffff0000, v54
	v_lshlrev_b32_e32 v54, 16, v55
	v_and_b32_e32 v55, 0xffff0000, v55
	s_nop 0
	v_mfma_f32_16x16x32_bf16 v[72:75], v[142:145], v[212:215], v[72:75]
	v_mfma_f32_16x16x32_bf16 v[48:51], v[124:127], v[212:215], v[48:51]
	v_mfma_f32_16x16x32_bf16 v[76:79], v[108:111], v[212:215], v[76:79]
	v_mfma_f32_16x16x32_bf16 v[52:55], v[92:95], v[212:215], v[52:55]
	v_mfma_f32_16x16x32_bf16 v[72:75], v[136:139], v[216:219], v[72:75]
	v_mfma_f32_16x16x32_bf16 v[48:51], v[120:123], v[216:219], v[48:51]
	v_mfma_f32_16x16x32_bf16 v[76:79], v[104:107], v[216:219], v[76:79]
	v_mfma_f32_16x16x32_bf16 v[52:55], v[88:91], v[216:219], v[52:55]
	v_mfma_f32_16x16x32_bf16 v[72:75], v[132:135], v[220:223], v[72:75]
	v_mfma_f32_16x16x32_bf16 v[48:51], v[116:119], v[220:223], v[48:51]
	v_mfma_f32_16x16x32_bf16 v[76:79], v[100:103], v[220:223], v[76:79]
	v_mfma_f32_16x16x32_bf16 v[52:55], v[84:87], v[220:223], v[52:55]
	v_mfma_f32_16x16x32_bf16 v[72:75], v[128:131], v[224:227], v[72:75]
	v_mfma_f32_16x16x32_bf16 v[48:51], v[112:115], v[224:227], v[48:51]
	v_mfma_f32_16x16x32_bf16 v[76:79], v[96:99], v[224:227], v[76:79]
	v_mfma_f32_16x16x32_bf16 v[52:55], v[80:83], v[224:227], v[52:55]
	v_add_u32_e32 v141, v47, v38
	v_add_u32_e32 v183, v47, v39
	v_add_u32_e32 v47, v47, v40
	ds_read_b128 v[80:83], v47 offset:36928
	ds_read_b128 v[84:87], v47 offset:36864
	ds_read_b128 v[88:91], v141 offset:52288
	ds_read_b128 v[92:95], v141 offset:52224
	ds_read_b128 v[96:99], v141 offset:49728
	ds_read_b128 v[100:103], v141 offset:49664
	ds_read_b128 v[104:107], v141 offset:47168
	ds_read_b128 v[108:111], v141 offset:47104
	ds_read_b128 v[112:115], v183 offset:36928
	ds_read_b128 v[116:119], v183 offset:36864
	ds_read_b128 v[120:123], v141 offset:42048
	ds_read_b128 v[124:127], v141 offset:41984
	ds_read_b128 v[128:131], v141 offset:39488
	ds_read_b128 v[132:135], v141 offset:39424
	ds_read_b128 v[136:139], v141 offset:36928
	ds_read_b128 v[142:145], v141 offset:36864
	s_waitcnt lgkmcnt(15)
; #define LAS __attribute__((address_space(3)))
; #define SC_BAR() do { asm volatile("s_waitcnt lgkmcnt(0)" ::: "memory"); __builtin_amdgcn_s_barrier(); asm volatile("" ::: "memory"); } while (0)
; #define PIN8(a) asm volatile("" : "+v"(a[0]), "+v"(a[1]), "+v"(a[2]), "+v"(a[3]), "+v"(a[4]), "+v"(a[5]), "+v"(a[6]), "+v"(a[7]))
; __device__ __forceinline__ void gdn_scan(const Params& P, LAS unsigned char* lds, int sb, int tid, int lane, int wave) {
;     ...
;         const int row = lane;
;         bf16* Y = (bf16*)((unsigned char*)P.out + OUT_Y);
;         float* SSQG = P.out;
;         SC_BAR();
; #pragma unroll 1
;         for (int n2 = 0; n2 <= NCH; ++n2) {
;             if (n2 > 0) {
;                 const int n = (n2 - 1) & 127, t = b * SEQ + n * 64 + row;
;                 const LAS float* src = (const LAS float*)(lds + SC_OT + ((n2 - 1) & 1) * (64 * 36 * 4)) + row * 36;
;     ...
;             for (int rho = 0; rho < 4; ++rho) Oc[rho] = __builtin_amdgcn_mfma_f32_16x16x32_bf16(fB[rho * 4 + s], Bs[s], Oc[rho], 0, 0, 0);
;         __builtin_amdgcn_sched_barrier(0);
; #pragma unroll
;         for (int rho = 0; rho < 4; ++rho)
; #pragma unroll
;             for (int s = 0; s < 2; ++s) fD[rho * 2 + s] = *(const LAS bf16x8*)(buf + SC_ATT + (16 * rho + col) * 144 + (32 * s + 8 * g) * 2);
;         bf16x8 Bv[2];
;         Bv[0] = pack_b(Vn[0], Vn[1]); Bv[1] = pack_b(Vn[2], Vn[3]);
; #pragma unroll
;         for (int tau = 0; tau < 8; ++tau) S[tau] = S[tau] * dec;
;         __builtin_amdgcn_sched_barrier(0);
;         PIN16(fC);
; #pragma unroll
;         for (int s = 0; s < 2; ++s)
; #pragma unroll
;             for (int tau = 0; tau < 8; ++tau) S[tau] = __builtin_amdgcn_mfma_f32_16x16x32_bf16(fC[tau * 2 + s], Bv[s], S[tau], 0, 0, 0);
;         __builtin_amdgcn_sched_barrier(0);
;         PIN8(fD);
; #pragma unroll
;         for (int s = 0; s < 2; ++s)
; #pragma unroll
;             for (int rho = 0; rho < 4; ++rho) Oc[rho] = __builtin_amdgcn_mfma_f32_16x16x32_bf16(fD[rho * 2 + s], Bv[s], Oc[rho], 0, 0, 0);
;         LAS float* ot = (LAS float*)(lds + SC_OT + par * (64 * 36 * 4)) + 16 * wave + col;
; #pragma unroll
;         for (int rho = 0; rho < 4; ++rho)
; #pragma unroll
;             for (int i = 0; i < 4; ++i) ot[(16 * rho + 4 * g + i) * 36] = Oc[rho][i];
;         SC_BAR();
	v_mfma_f32_16x16x32_bf16 v[208:211], v[208:211], v[212:215], 0
	v_pk_mul_f32 v[32:33], v[34:35], v[32:33] op_sel_hi:[0,1]
	v_mfma_f32_16x16x32_bf16 v[192:195], v[192:195], v[212:215], 0
	v_pk_mul_f32 v[30:31], v[34:35], v[30:31] op_sel_hi:[0,1]
	v_mfma_f32_16x16x32_bf16 v[174:177], v[174:177], v[212:215], 0
	v_pk_mul_f32 v[28:29], v[34:35], v[28:29] op_sel_hi:[0,1]
	v_mfma_f32_16x16x32_bf16 v[56:59], v[158:161], v[212:215], 0
	v_pk_mul_f32 v[26:27], v[34:35], v[26:27] op_sel_hi:[0,1]
	v_mfma_f32_16x16x32_bf16 v[158:161], v[204:207], v[216:219], v[208:211]
	v_pk_mul_f32 v[24:25], v[34:35], v[24:25] op_sel_hi:[0,1]
	v_mfma_f32_16x16x32_bf16 v[188:191], v[188:191], v[216:219], v[192:195]
	v_pk_mul_f32 v[22:23], v[34:35], v[22:23] op_sel_hi:[0,1]
	v_mfma_f32_16x16x32_bf16 v[170:173], v[170:173], v[216:219], v[174:177]
	v_pk_mul_f32 v[20:21], v[34:35], v[20:21] op_sel_hi:[0,1]
	v_mfma_f32_16x16x32_bf16 v[56:59], v[154:157], v[216:219], v[56:59]
	v_pk_mul_f32 v[18:19], v[34:35], v[18:19] op_sel_hi:[0,1]
	v_mfma_f32_16x16x32_bf16 v[60:63], v[200:203], v[220:223], v[158:161]
	v_pk_mul_f32 v[16:17], v[34:35], v[16:17] op_sel_hi:[0,1]
	v_cvt_pk_bf16_f32 v68, v72, v73
	v_mfma_f32_16x16x32_bf16 v[154:157], v[184:187], v[220:223], v[188:191]
	v_pk_mul_f32 v[14:15], v[34:35], v[14:15] op_sel_hi:[0,1]
	v_cvt_pk_bf16_f32 v69, v74, v75
	v_mfma_f32_16x16x32_bf16 v[158:161], v[166:169], v[220:223], v[170:173]
	v_pk_mul_f32 v[12:13], v[34:35], v[12:13] op_sel_hi:[0,1]
	v_cvt_pk_bf16_f32 v70, v48, v49
	v_mfma_f32_16x16x32_bf16 v[56:59], v[150:153], v[220:223], v[56:59]
	v_pk_mul_f32 v[10:11], v[34:35], v[10:11] op_sel_hi:[0,1]
	v_cvt_pk_bf16_f32 v71, v50, v51
	v_mfma_f32_16x16x32_bf16 v[60:63], v[196:199], v[224:227], v[60:63]
	v_pk_mul_f32 v[8:9], v[34:35], v[8:9] op_sel_hi:[0,1]
	v_cvt_pk_bf16_f32 v48, v76, v77
	v_mfma_f32_16x16x32_bf16 v[64:67], v[178:181], v[224:227], v[154:157]
	v_pk_mul_f32 v[6:7], v[34:35], v[6:7] op_sel_hi:[0,1]
	v_cvt_pk_bf16_f32 v49, v78, v79
	v_mfma_f32_16x16x32_bf16 v[150:153], v[162:165], v[224:227], v[158:161]
	v_pk_mul_f32 v[4:5], v[34:35], v[4:5] op_sel_hi:[0,1]
	v_cvt_pk_bf16_f32 v50, v52, v53
	v_mfma_f32_16x16x32_bf16 v[56:59], v[146:149], v[224:227], v[56:59]
	v_pk_mul_f32 v[2:3], v[34:35], v[2:3] op_sel_hi:[0,1]
	v_cvt_pk_bf16_f32 v51, v54, v55
	ds_read_b128 v[52:55], v183 offset:57408
	ds_read_b128 v[72:75], v183 offset:57344
	ds_read_b128 v[76:79], v141 offset:62528
	ds_read_b128 v[146:149], v141 offset:62464
	ds_read_b128 v[154:157], v141 offset:59968
	ds_read_b128 v[158:161], v141 offset:59904
	ds_read_b128 v[162:165], v141 offset:57408
	ds_read_b128 v[166:169], v141 offset:57344
	s_waitcnt lgkmcnt(8)
	s_nop 0
	v_mfma_f32_16x16x32_bf16 v[30:33], v[142:145], v[68:71], v[30:33]
	v_mfma_f32_16x16x32_bf16 v[26:29], v[132:135], v[68:71], v[26:29]
	v_mfma_f32_16x16x32_bf16 v[22:25], v[124:127], v[68:71], v[22:25]
	v_mfma_f32_16x16x32_bf16 v[18:21], v[116:119], v[68:71], v[18:21]
	v_mfma_f32_16x16x32_bf16 v[14:17], v[108:111], v[68:71], v[14:17]
	v_mfma_f32_16x16x32_bf16 v[10:13], v[100:103], v[68:71], v[10:13]
	v_mfma_f32_16x16x32_bf16 v[6:9], v[92:95], v[68:71], v[6:9]
	v_mfma_f32_16x16x32_bf16 v[2:5], v[84:87], v[68:71], v[2:5]
	v_mfma_f32_16x16x32_bf16 v[30:33], v[136:139], v[48:51], v[30:33]
	v_mfma_f32_16x16x32_bf16 v[26:29], v[128:131], v[48:51], v[26:29]
	v_mfma_f32_16x16x32_bf16 v[22:25], v[120:123], v[48:51], v[22:25]
	v_mfma_f32_16x16x32_bf16 v[18:21], v[112:115], v[48:51], v[18:21]
	v_mfma_f32_16x16x32_bf16 v[14:17], v[104:107], v[48:51], v[14:17]
	v_mfma_f32_16x16x32_bf16 v[10:13], v[96:99], v[48:51], v[10:13]
	v_mfma_f32_16x16x32_bf16 v[6:9], v[88:91], v[48:51], v[6:9]
	v_mfma_f32_16x16x32_bf16 v[2:5], v[80:83], v[48:51], v[2:5]
	s_waitcnt lgkmcnt(0)
	s_mulk_i32 s6, 0x2400
	v_mfma_f32_16x16x32_bf16 v[60:63], v[166:169], v[68:71], v[60:63]
	v_add_u32_e32 v34, s6, v35
	v_add_u32_e32 v47, v34, v41
	s_add_i32 s1, s1, 1
	v_mfma_f32_16x16x32_bf16 v[64:67], v[158:161], v[68:71], v[64:67]
	s_add_i32 s3, s3, 4
	s_cmpk_eq_i32 s1, 0x80
	v_mfma_f32_16x16x32_bf16 v[60:63], v[162:165], v[48:51], v[60:63]
	v_cvt_pk_bf16_f32 v212, v30, v31
	v_cvt_pk_bf16_f32 v213, v32, v33
	v_cvt_pk_bf16_f32 v214, v26, v27
	v_cvt_pk_bf16_f32 v215, v28, v29
	v_cvt_pk_bf16_f32 v216, v22, v23
	v_cvt_pk_bf16_f32 v217, v24, v25
	v_cvt_pk_bf16_f32 v218, v18, v19
	v_cvt_pk_bf16_f32 v219, v20, v21
	ds_write2_b32 v47, v60, v61 offset1:36
	ds_write_b32 v47, v62 offset:288
	v_mfma_f32_16x16x32_bf16 v[64:67], v[154:157], v[48:51], v[64:67]
	v_add_u32_e32 v60, v34, v42
	ds_write_b32 v60, v63
	v_add_u32_e32 v60, 0x800, v47
	v_mfma_f32_16x16x32_bf16 v[56:59], v[72:75], v[68:71], v[56:59]
	v_cvt_pk_bf16_f32 v220, v14, v15
	v_cvt_pk_bf16_f32 v221, v16, v17
	v_cvt_pk_bf16_f32 v222, v10, v11
	v_cvt_pk_bf16_f32 v223, v12, v13
	ds_write2_b32 v60, v64, v65 offset0:64 offset1:100
	v_mfma_f32_16x16x32_bf16 v[60:63], v[146:149], v[68:71], v[150:153]
	v_add_u32_e32 v64, v34, v43
	ds_write_b32 v47, v66 offset:2592
	ds_write_b32 v64, v67
	v_mfma_f32_16x16x32_bf16 v[60:63], v[76:79], v[48:51], v[60:63]
	v_add_u32_e32 v64, 0x1000, v47
	v_cvt_pk_bf16_f32 v224, v6, v7
	v_cvt_pk_bf16_f32 v225, v8, v9
	v_cvt_pk_bf16_f32 v226, v2, v3
	v_cvt_pk_bf16_f32 v227, v4, v5
	s_nop 2
	ds_write2_b32 v64, v60, v61 offset0:128 offset1:164
	ds_write_b32 v47, v62 offset:4896
	v_mfma_f32_16x16x32_bf16 v[48:51], v[52:55], v[48:51], v[56:59]
	v_add_u32_e32 v60, v34, v44
	ds_write_b32 v60, v63
	v_add_u32_e32 v60, 0x1800, v47
	v_add_u32_e32 v34, v34, v45
	s_nop 3
	ds_write2_b32 v60, v48, v49 offset0:192 offset1:228
	ds_write_b32 v47, v50 offset:7200
	ds_write_b32 v34, v51
	s_waitcnt lgkmcnt(0)
	s_barrier
	s_cbranch_scc0 .LBB0_2145
	s_branch .LBB0_2153
.LBB0_2147:
	v_readlane_b32 s1, v255, 6
	s_lshl_b32 s1, s1, 11
	s_and_b32 s8, s1, 0x2000
	s_add_i32 s1, 0, 0x23200
	s_and_b32 s3, s2, 3
	s_movk_i32 s4, 0x90
	v_mov_b32_e32 v1, s1
	v_mad_u32_u24 v1, v182, s4, v1
	s_ashr_i32 s1, s0, 31
	s_lshl_b32 s4, s3, 5
	s_add_u32 s6, s94, s4
	s_addc_u32 s7, s95, 0
	s_lshl_b64 s[4:5], s[0:1], 2
	s_add_u32 s4, s6, s4
	s_addc_u32 s5, s7, s5
	s_lshl_b32 s1, s3, 8
	s_add_u32 s1, s94, s1
	s_addc_u32 s3, s95, 0
	s_lshl_b32 s6, s0, 5
	s_ashr_i32 s7, s6, 31
	s_lshl_b64 s[6:7], s[6:7], 1
	s_add_u32 s1, s1, s6
	s_addc_u32 s3, s3, s7
	s_waitcnt lgkmcnt(0)
	s_barrier
	s_add_u32 s6, s1, 0x400000
	v_or_b32_e32 v2, s8, v182
	s_addc_u32 s7, s3, 0
	v_subrev_u32_e32 v2, 64, v2
	s_mov_b32 s1, -1
	v_mov_b32_e32 v3, 0
	s_movk_i32 s3, 0x7fff
	s_mov_b32 s10, 0xffff0000
	s_branch .LBB0_2149

; #define SC_WAITSET(set, cnt) asm volatile("s_waitcnt " cnt : "+v"(rs[set][0]), "+v"(rs[set][1]), "+v"(rs[set][2]), "+v"(rs[set][3]), "+v"(rs[set][4]), "+v"(rs[set][5]), "+v"(rs[set][6]), "+v"(rs[set][7]), \
;             "+v"(rs[set][8]), "+v"(rs[set][9]), "+v"(rs[set][10]), "+v"(rs[set][11]), "+v"(rs[set][12]), "+v"(rs[set][13]), "+v"(rs[set][14]) :: "memory")
; #define SC_NEED(c) do { unsigned sp_ = 0; while (*(volatile LAS unsigned*)(lds + SC_RDY) <= (unsigned)(c) && ++sp_ < (1u << 24)) __builtin_amdgcn_s_sleep(2); } while (0)
; __device__ __forceinline__ void gdn_scan(const Params& P, LAS unsigned char* lds, int sb, int tid, int lane, int wave) {
;     ...
;         constexpr int NP = 15, DEP = 3;
;         const int lt = tid - 256;
;         const unsigned voff = (unsigned)lt * 16u;
;         const int lA = (lt >> 4) * 272 + (lt & 15) * 16, lB = (lt >> 3) * 144 + (lt & 7) * 16, lU = SC_UFS + lt * 16;
;         v4u rs[DEP][NP];
;     ...
;         SC_NEED(0); SC_ISSUE(0, item0);
;         SC_WAITSET(0, "vmcnt(0)"); SC_WRITE(0, 0); SC_WAITSET(0, "lgkmcnt(0)");
;         SC_NEED(3); SC_ISSUE(1, item0 + 1); SC_ISSUE(2, item0 + 2); SC_ISSUE(0, item0 + 3);
.LBB0_2154:
	s_and_b64 vcc, exec, s[6:7]
	s_cbranch_vccz .LBB0_2205
	s_add_i32 s6, 0, 0x27a00
	v_mov_b32_e32 v1, s6
	ds_read_b32 v1, v1
	v_readlane_b32 s4, v254, 2
	v_readlane_b32 s1, v255, 6
	v_readlane_b32 s5, v254, 3
	s_lshl_b32 s3, s1, 7
	s_waitcnt lgkmcnt(0)
	v_cmp_ne_u32_e32 vcc, 0, v1
	v_readlane_b32 s4, v254, 20
	v_readlane_b32 s5, v254, 21
	s_cbranch_vccz .LBB0_2251
.LBB0_2156:
	v_add_u32_e32 v2, 0xffffff00, v0
	v_lshrrev_b32_e32 v3, 4, v2
	v_and_b32_e32 v4, 0xf0, v140
	s_movk_i32 s1, 0x120
	v_lshlrev_b32_e32 v1, 4, v2
	v_mad_i32_i24 v186, v3, s1, v4
	v_lshrrev_b32_e32 v2, 3, v2
	v_and_b32_e32 v3, 0x70, v140
	s_movk_i32 s1, 0xa0
	v_mad_i32_i24 v187, v2, s1, v3
	s_lshl_b32 s1, s3, 14
	s_add_u32 s7, s24, s1
	s_addc_u32 s42, s25, 0
	s_lshl_b32 s1, s3, 13
	s_add_u32 s4, s27, s1
	s_addc_u32 s5, s33, 0
	s_add_u32 s8, s7, 0x9c00000
	s_addc_u32 s9, s42, 0
	s_add_u32 s10, s7, 0x9c01000
	s_addc_u32 s11, s42, 0
	s_add_u32 s12, s7, 0x9c02000
	s_addc_u32 s13, s42, 0
	s_add_u32 s14, s7, 0x9c03000
	s_addc_u32 s15, s42, 0
	s_add_u32 s16, s7, 0xbc00000
	s_addc_u32 s17, s42, 0
	s_add_u32 s18, s7, 0xbc01000
	s_addc_u32 s19, s42, 0
	s_add_u32 s20, s7, 0xbc02000
	s_addc_u32 s21, s42, 0
	s_add_u32 s22, s7, 0xbc03000
	s_addc_u32 s23, s42, 0
	s_add_u32 s28, s7, 0xcc00000
	s_addc_u32 s29, s42, 0
	s_add_u32 s30, s7, 0xcc01000
	s_addc_u32 s31, s42, 0
	s_add_u32 s34, s7, 0xcc02000
	s_addc_u32 s35, s42, 0
	s_add_u32 s38, s7, 0xcc03000
	s_addc_u32 s39, s42, 0
	s_add_u32 s40, s4, 0x1000
	s_addc_u32 s41, s5, 0
	s_lshl_b32 s0, s0, 1
	s_ashr_i32 s1, s0, 31
	s_lshl_b64 s[0:1], s[0:1], 11
	s_add_u32 s7, s7, s0
	s_addc_u32 s43, s42, s1
	s_add_u32 s42, s7, 0xac00000
	s_nop 4
	global_load_dwordx4 v[2:5], v1, s[8:9] sc0 sc1
	global_load_dwordx4 v[6:9], v1, s[10:11] sc0 sc1
	global_load_dwordx4 v[10:13], v1, s[12:13] sc0 sc1
	global_load_dwordx4 v[14:17], v1, s[14:15] sc0 sc1
	global_load_dwordx4 v[18:21], v1, s[16:17] sc0 sc1
	global_load_dwordx4 v[22:25], v1, s[18:19] sc0 sc1
	global_load_dwordx4 v[26:29], v1, s[20:21] sc0 sc1
	global_load_dwordx4 v[30:33], v1, s[22:23] sc0 sc1
	s_addc_u32 s43, s43, 0
	s_nop 4
	global_load_dwordx4 v[34:37], v1, s[28:29] sc0 sc1
	global_load_dwordx4 v[38:41], v1, s[30:31] sc0 sc1
	global_load_dwordx4 v[42:45], v1, s[34:35] sc0 sc1
	global_load_dwordx4 v[46:49], v1, s[38:39] sc0 sc1
	global_load_dwordx4 v[50:53], v1, s[4:5] sc0 sc1
	global_load_dwordx4 v[54:57], v1, s[40:41] sc0 sc1
	global_load_dwordx4 v[58:61], v1, s[42:43] sc0 sc1
	v_add_u32_e32 v184, 0, v186
	s_waitcnt vmcnt(0)
	v_add_u32_e32 v188, 0, v1
	v_add_u32_e32 v185, 0, v187
	v_add_u32_e32 v183, 0x21000, v188
	ds_write_b128 v184, v[2:5]
	ds_write_b128 v184, v[18:21] offset:18432
	ds_write_b128 v185, v[34:37] offset:36864
	ds_write_b128 v184, v[6:9] offset:4608
	ds_write_b128 v184, v[22:25] offset:23040
	ds_write_b128 v185, v[38:41] offset:41984
	ds_write_b128 v184, v[10:13] offset:9216
	ds_write_b128 v184, v[26:29] offset:27648
	ds_write_b128 v185, v[42:45] offset:47104
	ds_write_b128 v184, v[14:17] offset:13824
	ds_write_b128 v184, v[30:33] offset:32256
	ds_write_b128 v185, v[46:49] offset:52224
	ds_write_b128 v185, v[50:53] offset:57344
	ds_write_b128 v185, v[54:57] offset:62464
	ds_write_b128 v183, v[58:61]
	s_waitcnt lgkmcnt(0)
	s_nop 0
	v_mov_b32_e32 v2, s6
	ds_read_b32 v2, v2
	s_waitcnt lgkmcnt(0)
	v_cmp_lt_u32_e32 vcc, 3, v2
	s_cbranch_vccnz .LBB0_2167
	s_mov_b32 s6, 0xfffff8
	s_add_i32 s7, 0, 0x27a00
	s_branch .LBB0_2159

; #define SC_BAR() do { asm volatile("s_waitcnt lgkmcnt(0)" ::: "memory"); __builtin_amdgcn_s_barrier(); asm volatile("" ::: "memory"); } while (0)
; #define SC_WAITSET(set, cnt) asm volatile("s_waitcnt " cnt : "+v"(rs[set][0]), "+v"(rs[set][1]), "+v"(rs[set][2]), "+v"(rs[set][3]), "+v"(rs[set][4]), "+v"(rs[set][5]), "+v"(rs[set][6]), "+v"(rs[set][7]), \
;             "+v"(rs[set][8]), "+v"(rs[set][9]), "+v"(rs[set][10]), "+v"(rs[set][11]), "+v"(rs[set][12]), "+v"(rs[set][13]), "+v"(rs[set][14]) :: "memory")
; #define SC_NEED(c) do { unsigned sp_ = 0; while (*(volatile LAS unsigned*)(lds + SC_RDY) <= (unsigned)(c) && ++sp_ < (1u << 24)) __builtin_amdgcn_s_sleep(2); } while (0)
; __device__ __forceinline__ void gdn_scan(const Params& P, LAS unsigned char* lds, int sb, int tid, int lane, int wave) {
;     ...
;         SC_NEED(0); SC_ISSUE(0, item0);
;         SC_WAITSET(0, "vmcnt(0)"); SC_WRITE(0, 0); SC_WAITSET(0, "lgkmcnt(0)");
;         SC_NEED(3); SC_ISSUE(1, item0 + 1); SC_ISSUE(2, item0 + 2); SC_ISSUE(0, item0 + 3);
;         SC_BAR();
.LBB0_2167:
	v_readlane_b32 s4, v254, 56
	v_readlane_b32 s5, v254, 57
	s_or_b32 s4, s3, 1
	s_lshl_b32 s5, s4, 14
	s_add_u32 s5, s24, s5
	s_addc_u32 s6, s25, 0
	s_lshl_b32 s4, s4, 13
	s_add_u32 s94, s27, s4
	s_addc_u32 s95, s33, 0
	s_add_u32 s66, s5, 0x9c00000
	s_addc_u32 s67, s6, 0
	s_add_u32 s70, s5, 0x9c01000
	s_addc_u32 s71, s6, 0
	s_add_u32 s76, s5, 0x9c02000
	s_addc_u32 s77, s6, 0
	s_add_u32 s82, s5, 0x9c03000
	s_addc_u32 s83, s6, 0
	s_add_u32 s84, s5, 0xbc00000
	s_addc_u32 s85, s6, 0
	s_add_u32 s86, s5, 0xbc01000
	s_addc_u32 s87, s6, 0
	s_add_u32 s90, s5, 0xbc02000
	s_addc_u32 s91, s6, 0
	s_add_u32 s28, s5, 0xbc03000
	s_addc_u32 s29, s6, 0
	s_add_u32 s96, s5, 0xcc00000
	s_addc_u32 s97, s6, 0
	s_add_u32 s52, s5, 0xcc01000
	s_addc_u32 s53, s6, 0
	s_add_u32 s38, s5, 0xcc02000
	s_addc_u32 s39, s6, 0
	s_add_u32 s30, s5, 0xcc03000
	s_addc_u32 s31, s6, 0
	s_add_u32 s22, s94, 0x1000
	s_addc_u32 s23, s95, 0
	s_add_u32 s4, s5, s0
	s_addc_u32 s5, s6, s1
	s_add_u32 s34, s4, 0xac00000
	s_addc_u32 s35, s5, 0
	s_or_b32 s4, s3, 2
	s_lshl_b32 s5, s4, 14
	s_add_u32 s5, s24, s5
	s_addc_u32 s6, s25, 0
	s_lshl_b32 s4, s4, 13
	s_add_u32 s16, s27, s4
	s_addc_u32 s17, s33, 0
	s_add_u32 s40, s5, 0x9c00000
	s_addc_u32 s41, s6, 0
	s_add_u32 s42, s5, 0x9c01000
	s_addc_u32 s43, s6, 0
	s_add_u32 s44, s5, 0x9c02000
	s_addc_u32 s45, s6, 0
	s_add_u32 s46, s5, 0x9c03000
	s_addc_u32 s47, s6, 0
	s_add_u32 s48, s5, 0xbc00000
	s_addc_u32 s49, s6, 0
	s_add_u32 s56, s5, 0xbc01000
	s_addc_u32 s57, s6, 0
	s_add_u32 s60, s5, 0xbc02000
	s_addc_u32 s61, s6, 0
	s_add_u32 s64, s5, 0xbc03000
	s_addc_u32 s65, s6, 0
	s_add_u32 s58, s5, 0xcc00000
	s_addc_u32 s59, s6, 0
	s_add_u32 s62, s5, 0xcc01000
	s_addc_u32 s63, s6, 0
	s_add_u32 s68, s5, 0xcc02000
	s_addc_u32 s69, s6, 0
	s_add_u32 s78, s5, 0xcc03000
	s_addc_u32 s79, s6, 0
	s_add_u32 s88, s16, 0x1000
	s_addc_u32 s89, s17, 0
	s_add_u32 s4, s5, s0
	s_addc_u32 s5, s6, s1
	s_add_u32 s92, s4, 0xac00000
	s_addc_u32 s93, s5, 0
	s_or_b32 s4, s3, 3
	s_lshl_b32 s5, s4, 14
	s_add_u32 s6, s24, s5
	s_addc_u32 s7, s25, 0
	s_lshl_b32 s4, s4, 13
	s_add_u32 s4, s27, s4
	s_addc_u32 s5, s33, 0
	s_add_u32 s36, s6, 0x9c00000
	s_addc_u32 s37, s7, 0
	s_add_u32 s8, s6, 0x9c01000
	s_addc_u32 s9, s7, 0
	s_add_u32 s10, s6, 0x9c02000
	s_addc_u32 s11, s7, 0
	s_add_u32 s12, s6, 0x9c03000
	s_addc_u32 s13, s7, 0
	s_add_u32 s14, s6, 0xbc00000
	s_addc_u32 s15, s7, 0
	s_add_u32 s18, s6, 0xbc01000
	s_addc_u32 s19, s7, 0
	s_add_u32 s20, s6, 0xbc02000
	s_addc_u32 s21, s7, 0
	s_nop 4
	global_load_dwordx4 v[66:69], v1, s[66:67] sc0 sc1
	global_load_dwordx4 v[70:73], v1, s[70:71] sc0 sc1
	global_load_dwordx4 v[74:77], v1, s[76:77] sc0 sc1
	global_load_dwordx4 v[78:81], v1, s[82:83] sc0 sc1
	global_load_dwordx4 v[82:85], v1, s[84:85] sc0 sc1
	global_load_dwordx4 v[86:89], v1, s[86:87] sc0 sc1
	global_load_dwordx4 v[90:93], v1, s[90:91] sc0 sc1
	global_load_dwordx4 v[94:97], v1, s[28:29] sc0 sc1
	s_add_u32 s84, s6, 0xbc03000
	s_addc_u32 s85, s7, 0
	s_add_u32 s66, s6, 0xcc00000
	s_addc_u32 s67, s7, 0
	s_add_u32 s70, s6, 0xcc01000
	s_addc_u32 s71, s7, 0
	s_add_u32 s76, s6, 0xcc02000
	s_addc_u32 s77, s7, 0
	s_add_u32 s82, s6, 0xcc03000
	s_addc_u32 s83, s7, 0
	s_add_u32 s86, s4, 0x1000
	s_addc_u32 s87, s5, 0
	s_nop 4
	global_load_dwordx4 v[154:157], v1, s[96:97] sc0 sc1
	global_load_dwordx4 v[158:161], v1, s[52:53] sc0 sc1
	global_load_dwordx4 v[162:165], v1, s[38:39] sc0 sc1
	global_load_dwordx4 v[166:169], v1, s[30:31] sc0 sc1
	global_load_dwordx4 v[170:173], v1, s[94:95] sc0 sc1
	global_load_dwordx4 v[174:177], v1, s[22:23] sc0 sc1
	global_load_dwordx4 v[178:181], v1, s[34:35] sc0 sc1
	s_add_u32 s6, s6, s0
	s_nop 4
	global_load_dwordx4 v[2:5], v1, s[40:41] sc0 sc1
	global_load_dwordx4 v[6:9], v1, s[42:43] sc0 sc1
	global_load_dwordx4 v[10:13], v1, s[44:45] sc0 sc1
	global_load_dwordx4 v[14:17], v1, s[46:47] sc0 sc1
	global_load_dwordx4 v[18:21], v1, s[48:49] sc0 sc1
	global_load_dwordx4 v[22:25], v1, s[56:57] sc0 sc1
	global_load_dwordx4 v[26:29], v1, s[60:61] sc0 sc1
	global_load_dwordx4 v[30:33], v1, s[64:65] sc0 sc1
	s_addc_u32 s7, s7, s1
	s_nop 4
	global_load_dwordx4 v[98:101], v1, s[58:59] sc0 sc1
	global_load_dwordx4 v[102:105], v1, s[62:63] sc0 sc1
	global_load_dwordx4 v[106:109], v1, s[68:69] sc0 sc1
	global_load_dwordx4 v[110:113], v1, s[78:79] sc0 sc1
	global_load_dwordx4 v[114:117], v1, s[16:17] sc0 sc1
	global_load_dwordx4 v[118:121], v1, s[88:89] sc0 sc1
	global_load_dwordx4 v[122:125], v1, s[92:93] sc0 sc1
	s_add_u32 s90, s6, 0xac00000
	s_nop 4
	global_load_dwordx4 v[34:37], v1, s[36:37] sc0 sc1
	global_load_dwordx4 v[38:41], v1, s[8:9] sc0 sc1
	global_load_dwordx4 v[42:45], v1, s[10:11] sc0 sc1
	global_load_dwordx4 v[46:49], v1, s[12:13] sc0 sc1
	global_load_dwordx4 v[50:53], v1, s[14:15] sc0 sc1
	global_load_dwordx4 v[54:57], v1, s[18:19] sc0 sc1
	global_load_dwordx4 v[58:61], v1, s[20:21] sc0 sc1
	global_load_dwordx4 v[62:65], v1, s[84:85] sc0 sc1
	s_addc_u32 s91, s7, 0
	s_nop 4
	global_load_dwordx4 v[126:129], v1, s[66:67] sc0 sc1
	global_load_dwordx4 v[130:133], v1, s[70:71] sc0 sc1
	global_load_dwordx4 v[134:137], v1, s[76:77] sc0 sc1
	global_load_dwordx4 v[138:141], v1, s[82:83] sc0 sc1
	global_load_dwordx4 v[142:145], v1, s[4:5] sc0 sc1
	global_load_dwordx4 v[146:149], v1, s[86:87] sc0 sc1
	global_load_dwordx4 v[150:153], v1, s[90:91] sc0 sc1
	s_waitcnt lgkmcnt(0)
	s_barrier
	s_mov_b32 s55, 0
	s_add_i32 s28, 0, 0x27a00
	s_mov_b32 s31, 0
	s_mov_b32 s29, 0
	s_branch .LBB0_2169
; #define SC_BAR() do { asm volatile("s_waitcnt lgkmcnt(0)" ::: "memory"); __builtin_amdgcn_s_barrier(); asm volatile("" ::: "memory"); } while (0)
; #define SC_WAITSET(set, cnt) asm volatile("s_waitcnt " cnt : "+v"(rs[set][0]), "+v"(rs[set][1]), "+v"(rs[set][2]), "+v"(rs[set][3]), "+v"(rs[set][4]), "+v"(rs[set][5]), "+v"(rs[set][6]), "+v"(rs[set][7]), \
;             "+v"(rs[set][8]), "+v"(rs[set][9]), "+v"(rs[set][10]), "+v"(rs[set][11]), "+v"(rs[set][12]), "+v"(rs[set][13]), "+v"(rs[set][14]) :: "memory")
; #define SC_NEED(c) do { unsigned sp_ = 0; while (*(volatile LAS unsigned*)(lds + SC_RDY) <= (unsigned)(c) && ++sp_ < (1u << 24)) __builtin_amdgcn_s_sleep(2); } while (0)
; #define SC_INTERVAL(set) do { SC_WAITSET(set, "vmcnt(30)"); SC_WRITE(set, (n2 + 1) & 1); SC_WAITSET(set, "lgkmcnt(0)"); if (n2 + 1 + DEP < 128) SC_NEED(n2 + 1 + DEP); SC_ISSUE(set, item0 + ((n2 + 1 + DEP) & 127)); SC_BAR(); ++n2; } while (0)
; __device__ __forceinline__ void gdn_scan(const Params& P, LAS unsigned char* lds, int sb, int tid, int lane, int wave) {
;     ...
;         SC_NEED(0); SC_ISSUE(0, item0);
;         SC_WAITSET(0, "vmcnt(0)"); SC_WRITE(0, 0); SC_WAITSET(0, "lgkmcnt(0)");
;         SC_NEED(3); SC_ISSUE(1, item0 + 1); SC_ISSUE(2, item0 + 2); SC_ISSUE(0, item0 + 3);
;         SC_BAR();
;         int n2 = 0;
;     ...
; #pragma unroll 1
;         for (int it = 0; it < NCH / 3; ++it) { SC_INTERVAL(1); SC_INTERVAL(2); SC_INTERVAL(0); }
.LBB0_2168:
	s_and_b32 s6, s34, 0x7f
	s_or_b32 s6, s6, s3
	s_lshl_b32 s7, s6, 14
	s_add_u32 s30, s24, s7
	s_addc_u32 s54, s25, 0
	s_lshl_b32 s6, s6, 13
	s_add_u32 s6, s27, s6
	s_addc_u32 s7, s33, 0
	s_add_u32 s22, s30, 0x9c00000
	s_addc_u32 s23, s54, 0
	s_add_u32 s34, s30, 0x9c01000
	s_addc_u32 s35, s54, 0
	s_add_u32 s38, s30, 0x9c02000
	s_addc_u32 s39, s54, 0
	s_add_u32 s52, s30, 0x9c03000
	s_addc_u32 s53, s54, 0
	s_add_u32 s72, s30, 0xbc00000
	s_addc_u32 s73, s54, 0
	s_add_u32 s74, s30, 0xbc01000
	s_addc_u32 s75, s54, 0
	s_add_u32 s94, s30, 0xbc02000
	s_addc_u32 s95, s54, 0
	s_add_u32 s96, s30, 0xbc03000
	s_addc_u32 s97, s54, 0
	s_nop 4
	ds_write_b128 v189, v[34:37]
	ds_write_b128 v189, v[38:41] offset:4608
	global_load_dwordx4 v[34:37], v1, s[22:23] sc0 sc1
	ds_write_b128 v189, v[42:45] offset:9216
	global_load_dwordx4 v[38:41], v1, s[34:35] sc0 sc1
	ds_write_b128 v189, v[46:49] offset:13824
	global_load_dwordx4 v[42:45], v1, s[38:39] sc0 sc1
	ds_write_b128 v189, v[50:53] offset:18432
	global_load_dwordx4 v[46:49], v1, s[52:53] sc0 sc1
	ds_write_b128 v189, v[54:57] offset:23040
	global_load_dwordx4 v[50:53], v1, s[72:73] sc0 sc1
	ds_write_b128 v189, v[58:61] offset:27648
	global_load_dwordx4 v[54:57], v1, s[74:75] sc0 sc1
	ds_write_b128 v189, v[62:65] offset:32256
	global_load_dwordx4 v[58:61], v1, s[94:95] sc0 sc1
	ds_write_b128 v190, v[126:129] offset:36864
	global_load_dwordx4 v[62:65], v1, s[96:97] sc0 sc1
	s_add_u32 s22, s30, 0xcc00000
	s_addc_u32 s23, s54, 0
	s_add_u32 s34, s30, 0xcc01000
	s_addc_u32 s35, s54, 0
	s_add_u32 s38, s30, 0xcc02000
	s_addc_u32 s39, s54, 0
	s_add_u32 s52, s30, 0xcc03000
	s_addc_u32 s53, s54, 0
	s_add_u32 s72, s6, 0x1000
	s_addc_u32 s73, s7, 0
	s_add_u32 s30, s30, s0
	s_addc_u32 s54, s54, s1
	s_add_u32 s74, s30, 0xac00000
	s_addc_u32 s75, s54, 0
	s_nop 4
	ds_write_b128 v190, v[130:133] offset:41984
	global_load_dwordx4 v[126:129], v1, s[22:23] sc0 sc1
	ds_write_b128 v190, v[134:137] offset:47104
	global_load_dwordx4 v[130:133], v1, s[34:35] sc0 sc1
	ds_write_b128 v190, v[138:141] offset:52224
	global_load_dwordx4 v[134:137], v1, s[38:39] sc0 sc1
	ds_write_b128 v190, v[142:145] offset:57344
	global_load_dwordx4 v[138:141], v1, s[52:53] sc0 sc1
	ds_write_b128 v190, v[146:149] offset:62464
	global_load_dwordx4 v[142:145], v1, s[6:7] sc0 sc1
	ds_write_b128 v201, v[150:153]
	global_load_dwordx4 v[146:149], v1, s[72:73] sc0 sc1
	global_load_dwordx4 v[150:153], v1, s[74:75] sc0 sc1
	s_waitcnt lgkmcnt(0)
	s_barrier
	s_add_i32 s29, s29, 1
	s_cmp_eq_u32 s29, 42
	s_cbranch_scc1 .LBB0_2204
.LBB0_2169:
	s_mov_b32 s30, s31
	s_and_b32 s31, s31, 1
	s_waitcnt vmcnt(30)
	s_xor_b32 s6, s31, 1
	s_mul_i32 s7, s6, 0x10800
	s_add_i32 s7, s7, 0
	v_add_u32_e32 v189, s7, v186
	v_add_u32_e32 v190, s7, v187
	v_lshl_add_u32 v201, s6, 12, v183
	s_add_i32 s34, s30, 4
	v_mov_b32_e32 v200, s28
	ds_read_b32 v200, v200
	s_waitcnt lgkmcnt(0)
	v_cmp_lt_u32_e32 vcc, s34, v200
	s_cbranch_vccnz .LBB0_2180
	s_mov_b32 s35, 0xfffff8
	s_branch .LBB0_2172

; #define SC_BAR() do { asm volatile("s_waitcnt lgkmcnt(0)" ::: "memory"); __builtin_amdgcn_s_barrier(); asm volatile("" ::: "memory"); } while (0)
; #define SC_WAITSET(set, cnt) asm volatile("s_waitcnt " cnt : "+v"(rs[set][0]), "+v"(rs[set][1]), "+v"(rs[set][2]), "+v"(rs[set][3]), "+v"(rs[set][4]), "+v"(rs[set][5]), "+v"(rs[set][6]), "+v"(rs[set][7]), \
;             "+v"(rs[set][8]), "+v"(rs[set][9]), "+v"(rs[set][10]), "+v"(rs[set][11]), "+v"(rs[set][12]), "+v"(rs[set][13]), "+v"(rs[set][14]) :: "memory")
; #define SC_NEED(c) do { unsigned sp_ = 0; while (*(volatile LAS unsigned*)(lds + SC_RDY) <= (unsigned)(c) && ++sp_ < (1u << 24)) __builtin_amdgcn_s_sleep(2); } while (0)
; #define SC_INTERVAL(set) do { SC_WAITSET(set, "vmcnt(30)"); SC_WRITE(set, (n2 + 1) & 1); SC_WAITSET(set, "lgkmcnt(0)"); if (n2 + 1 + DEP < 128) SC_NEED(n2 + 1 + DEP); SC_ISSUE(set, item0 + ((n2 + 1 + DEP) & 127)); SC_BAR(); ++n2; } while (0)
; __device__ __forceinline__ void gdn_scan(const Params& P, LAS unsigned char* lds, int sb, int tid, int lane, int wave) {
;     ...
;         SC_NEED(0); SC_ISSUE(0, item0);
;         SC_WAITSET(0, "vmcnt(0)"); SC_WRITE(0, 0); SC_WAITSET(0, "lgkmcnt(0)");
;         SC_NEED(3); SC_ISSUE(1, item0 + 1); SC_ISSUE(2, item0 + 2); SC_ISSUE(0, item0 + 3);
;         SC_BAR();
;         int n2 = 0;
;     ...
; #pragma unroll 1
;         for (int it = 0; it < NCH / 3; ++it) { SC_INTERVAL(1); SC_INTERVAL(2); SC_INTERVAL(0); }
.LBB0_2180:
	s_or_b32 s54, s34, s3
	s_lshl_b64 s[22:23], s[54:55], 14
	s_add_u32 vcc_lo, s24, s22
	s_addc_u32 vcc_hi, s25, s23
	s_lshl_b64 s[22:23], s[54:55], 13
	s_add_u32 s22, s27, s22
	s_addc_u32 s23, s33, s23
	s_add_u32 s34, vcc_lo, 0x9c00000
	s_addc_u32 s35, vcc_hi, 0
	s_add_u32 s38, vcc_lo, 0x9c01000
	s_addc_u32 s39, vcc_hi, 0
	s_add_u32 s52, vcc_lo, 0x9c02000
	s_addc_u32 s53, vcc_hi, 0
	s_add_u32 s72, vcc_lo, 0x9c03000
	s_addc_u32 s73, vcc_hi, 0
	s_add_u32 s74, vcc_lo, 0xbc00000
	s_addc_u32 s75, vcc_hi, 0
	s_add_u32 s94, vcc_lo, 0xbc01000
	s_addc_u32 s95, vcc_hi, 0
	s_add_u32 s96, vcc_lo, 0xbc02000
	s_addc_u32 s97, vcc_hi, 0
	s_add_u32 s6, vcc_lo, 0xbc03000
	s_addc_u32 s7, vcc_hi, 0
	s_nop 4
	ds_write_b128 v189, v[66:69]
	ds_write_b128 v189, v[70:73] offset:4608
	global_load_dwordx4 v[66:69], v1, s[34:35] sc0 sc1
	ds_write_b128 v189, v[74:77] offset:9216
	global_load_dwordx4 v[70:73], v1, s[38:39] sc0 sc1
	ds_write_b128 v189, v[78:81] offset:13824
	global_load_dwordx4 v[74:77], v1, s[52:53] sc0 sc1
	ds_write_b128 v189, v[82:85] offset:18432
	global_load_dwordx4 v[78:81], v1, s[72:73] sc0 sc1
	ds_write_b128 v189, v[86:89] offset:23040
	global_load_dwordx4 v[82:85], v1, s[74:75] sc0 sc1
	ds_write_b128 v189, v[90:93] offset:27648
	global_load_dwordx4 v[86:89], v1, s[94:95] sc0 sc1
	ds_write_b128 v189, v[94:97] offset:32256
	global_load_dwordx4 v[90:93], v1, s[96:97] sc0 sc1
	ds_write_b128 v190, v[154:157] offset:36864
	global_load_dwordx4 v[94:97], v1, s[6:7] sc0 sc1
	s_add_u32 s6, vcc_lo, 0xcc00000
	s_addc_u32 s7, vcc_hi, 0
	s_add_u32 s34, vcc_lo, 0xcc01000
	s_addc_u32 s35, vcc_hi, 0
	s_add_u32 s38, vcc_lo, 0xcc02000
	s_addc_u32 s39, vcc_hi, 0
	s_add_u32 s52, vcc_lo, 0xcc03000
	s_addc_u32 s53, vcc_hi, 0
	s_add_u32 s72, s22, 0x1000
	s_addc_u32 s73, s23, 0
	s_add_u32 s54, vcc_lo, s0
	s_addc_u32 s75, vcc_hi, s1
	s_add_u32 s74, s54, 0xac00000
	s_addc_u32 s75, s75, 0
	s_nop 4
	ds_write_b128 v190, v[158:161] offset:41984
	global_load_dwordx4 v[154:157], v1, s[6:7] sc0 sc1
	ds_write_b128 v190, v[162:165] offset:47104
	global_load_dwordx4 v[158:161], v1, s[34:35] sc0 sc1
	ds_write_b128 v190, v[166:169] offset:52224
	global_load_dwordx4 v[162:165], v1, s[38:39] sc0 sc1
	ds_write_b128 v190, v[170:173] offset:57344
	global_load_dwordx4 v[166:169], v1, s[52:53] sc0 sc1
	ds_write_b128 v190, v[174:177] offset:62464
	global_load_dwordx4 v[170:173], v1, s[22:23] sc0 sc1
	ds_write_b128 v201, v[178:181]
	global_load_dwordx4 v[174:177], v1, s[72:73] sc0 sc1
	global_load_dwordx4 v[178:181], v1, s[74:75] sc0 sc1
	s_waitcnt lgkmcnt(0)
	s_barrier
	s_waitcnt vmcnt(30)
	s_mul_i32 s6, s31, 0x10800
	s_add_i32 s6, s6, 0
	v_add_u32_e32 v189, s6, v186
	v_add_u32_e32 v190, s6, v187
	v_lshl_add_u32 v201, s31, 12, v183
	s_add_i32 s31, s30, 5
	s_cmpk_gt_u32 s30, 0x7a
	s_cbranch_scc1 .LBB0_2192
	v_mov_b32_e32 v200, s28
	ds_read_b32 v200, v200
	s_waitcnt lgkmcnt(0)
	v_cmp_lt_u32_e32 vcc, s31, v200
	s_cbranch_vccnz .LBB0_2192
	s_mov_b32 s34, 0xfffff8
	s_branch .LBB0_2184

; #define SC_BAR() do { asm volatile("s_waitcnt lgkmcnt(0)" ::: "memory"); __builtin_amdgcn_s_barrier(); asm volatile("" ::: "memory"); } while (0)
; #define SC_WAITSET(set, cnt) asm volatile("s_waitcnt " cnt : "+v"(rs[set][0]), "+v"(rs[set][1]), "+v"(rs[set][2]), "+v"(rs[set][3]), "+v"(rs[set][4]), "+v"(rs[set][5]), "+v"(rs[set][6]), "+v"(rs[set][7]), \
;             "+v"(rs[set][8]), "+v"(rs[set][9]), "+v"(rs[set][10]), "+v"(rs[set][11]), "+v"(rs[set][12]), "+v"(rs[set][13]), "+v"(rs[set][14]) :: "memory")
; #define SC_NEED(c) do { unsigned sp_ = 0; while (*(volatile LAS unsigned*)(lds + SC_RDY) <= (unsigned)(c) && ++sp_ < (1u << 24)) __builtin_amdgcn_s_sleep(2); } while (0)
; #define SC_INTERVAL(set) do { SC_WAITSET(set, "vmcnt(30)"); SC_WRITE(set, (n2 + 1) & 1); SC_WAITSET(set, "lgkmcnt(0)"); if (n2 + 1 + DEP < 128) SC_NEED(n2 + 1 + DEP); SC_ISSUE(set, item0 + ((n2 + 1 + DEP) & 127)); SC_BAR(); ++n2; } while (0)
; __device__ __forceinline__ void gdn_scan(const Params& P, LAS unsigned char* lds, int sb, int tid, int lane, int wave) {
;     ...
;         SC_NEED(0); SC_ISSUE(0, item0);
;         SC_WAITSET(0, "vmcnt(0)"); SC_WRITE(0, 0); SC_WAITSET(0, "lgkmcnt(0)");
;         SC_NEED(3); SC_ISSUE(1, item0 + 1); SC_ISSUE(2, item0 + 2); SC_ISSUE(0, item0 + 3);
;         SC_BAR();
;         int n2 = 0;
;     ...
; #pragma unroll 1
;         for (int it = 0; it < NCH / 3; ++it) { SC_INTERVAL(1); SC_INTERVAL(2); SC_INTERVAL(0); }
.LBB0_2192:
	s_and_b32 s6, s31, 0x7f
	s_or_b32 s6, s6, s3
	s_lshl_b32 s7, s6, 14
	s_add_u32 s31, s24, s7
	s_addc_u32 s54, s25, 0
	s_lshl_b32 s6, s6, 13
	s_add_u32 s6, s27, s6
	s_addc_u32 s7, s33, 0
	s_add_u32 s22, s31, 0x9c00000
	s_addc_u32 s23, s54, 0
	s_add_u32 s34, s31, 0x9c01000
	s_addc_u32 s35, s54, 0
	s_add_u32 s38, s31, 0x9c02000
	s_addc_u32 s39, s54, 0
	s_add_u32 s52, s31, 0x9c03000
	s_addc_u32 s53, s54, 0
	s_add_u32 s72, s31, 0xbc00000
	s_addc_u32 s73, s54, 0
	s_add_u32 s74, s31, 0xbc01000
	s_addc_u32 s75, s54, 0
	s_add_u32 s94, s31, 0xbc02000
	s_addc_u32 s95, s54, 0
	s_add_u32 s96, s31, 0xbc03000
	s_addc_u32 s97, s54, 0
	s_nop 4
	ds_write_b128 v189, v[2:5]
	ds_write_b128 v189, v[6:9] offset:4608
	global_load_dwordx4 v[2:5], v1, s[22:23] sc0 sc1
	ds_write_b128 v189, v[10:13] offset:9216
	global_load_dwordx4 v[6:9], v1, s[34:35] sc0 sc1
	ds_write_b128 v189, v[14:17] offset:13824
	global_load_dwordx4 v[10:13], v1, s[38:39] sc0 sc1
	ds_write_b128 v189, v[18:21] offset:18432
	global_load_dwordx4 v[14:17], v1, s[52:53] sc0 sc1
	ds_write_b128 v189, v[22:25] offset:23040
	global_load_dwordx4 v[18:21], v1, s[72:73] sc0 sc1
	ds_write_b128 v189, v[26:29] offset:27648
	global_load_dwordx4 v[22:25], v1, s[74:75] sc0 sc1
	ds_write_b128 v189, v[30:33] offset:32256
	global_load_dwordx4 v[26:29], v1, s[94:95] sc0 sc1
	ds_write_b128 v190, v[98:101] offset:36864
	global_load_dwordx4 v[30:33], v1, s[96:97] sc0 sc1
	s_add_u32 s22, s31, 0xcc00000
	s_addc_u32 s23, s54, 0
	s_add_u32 s34, s31, 0xcc01000
	s_addc_u32 s35, s54, 0
	s_add_u32 s38, s31, 0xcc02000
	s_addc_u32 s39, s54, 0
	s_add_u32 s52, s31, 0xcc03000
	s_addc_u32 s53, s54, 0
	s_add_u32 s72, s6, 0x1000
	s_addc_u32 s73, s7, 0
	s_add_u32 s31, s31, s0
	s_addc_u32 s54, s54, s1
	s_add_u32 s74, s31, 0xac00000
	s_addc_u32 s75, s54, 0
	s_nop 4
	ds_write_b128 v190, v[102:105] offset:41984
	global_load_dwordx4 v[98:101], v1, s[22:23] sc0 sc1
	ds_write_b128 v190, v[106:109] offset:47104
	global_load_dwordx4 v[102:105], v1, s[34:35] sc0 sc1
	ds_write_b128 v190, v[110:113] offset:52224
	global_load_dwordx4 v[106:109], v1, s[38:39] sc0 sc1
	ds_write_b128 v190, v[114:117] offset:57344
	global_load_dwordx4 v[110:113], v1, s[52:53] sc0 sc1
	ds_write_b128 v190, v[118:121] offset:62464
	global_load_dwordx4 v[114:117], v1, s[6:7] sc0 sc1
	ds_write_b128 v201, v[122:125]
	global_load_dwordx4 v[118:121], v1, s[72:73] sc0 sc1
	global_load_dwordx4 v[122:125], v1, s[74:75] sc0 sc1
	s_waitcnt lgkmcnt(0)
	s_barrier
	s_add_i32 s31, s30, 3
	s_waitcnt vmcnt(30)
	s_and_b32 s6, s31, 1
	s_mul_i32 s7, s6, 0x10800
	s_add_i32 s7, s7, 0
	v_add_u32_e32 v189, s7, v186
	v_add_u32_e32 v190, s7, v187
	v_lshl_add_u32 v201, s6, 12, v183
	s_add_i32 s34, s30, 6
	s_cmpk_gt_u32 s30, 0x79
	s_cbranch_scc1 .LBB0_2168
	v_mov_b32_e32 v200, s28
	ds_read_b32 v200, v200
	s_waitcnt lgkmcnt(0)
	v_cmp_lt_u32_e32 vcc, s34, v200
	s_cbranch_vccnz .LBB0_2168
	s_mov_b32 s30, 0xfffff8
	s_branch .LBB0_2196

; #define SC_BAR() do { asm volatile("s_waitcnt lgkmcnt(0)" ::: "memory"); __builtin_amdgcn_s_barrier(); asm volatile("" ::: "memory"); } while (0)
; #define SC_WAITSET(set, cnt) asm volatile("s_waitcnt " cnt : "+v"(rs[set][0]), "+v"(rs[set][1]), "+v"(rs[set][2]), "+v"(rs[set][3]), "+v"(rs[set][4]), "+v"(rs[set][5]), "+v"(rs[set][6]), "+v"(rs[set][7]), \
;             "+v"(rs[set][8]), "+v"(rs[set][9]), "+v"(rs[set][10]), "+v"(rs[set][11]), "+v"(rs[set][12]), "+v"(rs[set][13]), "+v"(rs[set][14]) :: "memory")
; #define SC_NEED(c) do { unsigned sp_ = 0; while (*(volatile LAS unsigned*)(lds + SC_RDY) <= (unsigned)(c) && ++sp_ < (1u << 24)) __builtin_amdgcn_s_sleep(2); } while (0)
; #define SC_INTERVAL(set) do { SC_WAITSET(set, "vmcnt(30)"); SC_WRITE(set, (n2 + 1) & 1); SC_WAITSET(set, "lgkmcnt(0)"); if (n2 + 1 + DEP < 128) SC_NEED(n2 + 1 + DEP); SC_ISSUE(set, item0 + ((n2 + 1 + DEP) & 127)); SC_BAR(); ++n2; } while (0)
; __device__ __forceinline__ void gdn_scan(const Params& P, LAS unsigned char* lds, int sb, int tid, int lane, int wave) {
;     ...
;         SC_NEED(0); SC_ISSUE(0, item0);
;         SC_WAITSET(0, "vmcnt(0)"); SC_WRITE(0, 0); SC_WAITSET(0, "lgkmcnt(0)");
;         SC_NEED(3); SC_ISSUE(1, item0 + 1); SC_ISSUE(2, item0 + 2); SC_ISSUE(0, item0 + 3);
;         SC_BAR();
;         int n2 = 0;
;     ...
; #pragma unroll 1
;         for (int it = 0; it < NCH / 3; ++it) { SC_INTERVAL(1); SC_INTERVAL(2); SC_INTERVAL(0); }
;         if (NCH % 3 >= 1) SC_INTERVAL(1);
;         if (NCH % 3 >= 2) SC_INTERVAL(2);
;         SC_WAITSET(0, "vmcnt(0)"); SC_WAITSET(1, "vmcnt(0)"); SC_WAITSET(2, "vmcnt(0)");
.LBB0_2204:
	s_waitcnt vmcnt(30)
	v_add_u32_e32 v186, 0x10800, v184
	v_add_u32_e32 v189, 0x19800, v185
	v_add_u32_e32 v187, 0x22000, v188
	v_add_u32_e32 v188, 0x15000, v184
	ds_write_b128 v186, v[66:69]
	ds_write_b128 v188, v[82:85]
	ds_write_b128 v189, v[154:157]
	ds_write_b128 v186, v[70:73] offset:4608
	ds_write_b128 v188, v[86:89] offset:4608
	ds_write_b128 v189, v[158:161] offset:5120
	ds_write_b128 v186, v[74:77] offset:9216
	ds_write_b128 v188, v[90:93] offset:9216
	ds_write_b128 v189, v[162:165] offset:10240
	ds_write_b128 v186, v[78:81] offset:13824
	ds_write_b128 v188, v[94:97] offset:13824
	ds_write_b128 v189, v[166:169] offset:15360
	v_add_u32_e32 v186, 0x1e800, v185
	ds_write_b128 v186, v[170:173]
	ds_write_b128 v186, v[174:177] offset:5120
	ds_write_b128 v187, v[178:181]
	s_waitcnt lgkmcnt(0)
	s_nop 0
	s_nop 4
	global_load_dwordx4 v[66:69], v1, s[40:41] sc0 sc1
	global_load_dwordx4 v[70:73], v1, s[42:43] sc0 sc1
	global_load_dwordx4 v[74:77], v1, s[44:45] sc0 sc1
	global_load_dwordx4 v[78:81], v1, s[46:47] sc0 sc1
	global_load_dwordx4 v[82:85], v1, s[48:49] sc0 sc1
	global_load_dwordx4 v[86:89], v1, s[56:57] sc0 sc1
	global_load_dwordx4 v[90:93], v1, s[60:61] sc0 sc1
	global_load_dwordx4 v[94:97], v1, s[64:65] sc0 sc1
	s_nop 4
	global_load_dwordx4 v[154:157], v1, s[58:59] sc0 sc1
	global_load_dwordx4 v[158:161], v1, s[62:63] sc0 sc1
	global_load_dwordx4 v[162:165], v1, s[68:69] sc0 sc1
	global_load_dwordx4 v[166:169], v1, s[78:79] sc0 sc1
	global_load_dwordx4 v[170:173], v1, s[16:17] sc0 sc1
	global_load_dwordx4 v[174:177], v1, s[88:89] sc0 sc1
	global_load_dwordx4 v[178:181], v1, s[92:93] sc0 sc1
	s_waitcnt lgkmcnt(0)
	s_barrier
	s_waitcnt vmcnt(30)
	ds_write_b128 v184, v[2:5]
	ds_write_b128 v184, v[18:21] offset:18432
	ds_write_b128 v185, v[98:101] offset:36864
	ds_write_b128 v184, v[6:9] offset:4608
	ds_write_b128 v184, v[22:25] offset:23040
	ds_write_b128 v185, v[102:105] offset:41984
	ds_write_b128 v184, v[10:13] offset:9216
	ds_write_b128 v184, v[26:29] offset:27648
	ds_write_b128 v185, v[106:109] offset:47104
	ds_write_b128 v184, v[14:17] offset:13824
	ds_write_b128 v184, v[30:33] offset:32256
	ds_write_b128 v185, v[110:113] offset:52224
	ds_write_b128 v185, v[114:117] offset:57344
	ds_write_b128 v185, v[118:121] offset:62464
	ds_write_b128 v183, v[122:125]
	s_waitcnt lgkmcnt(0)
	s_nop 0
	s_nop 4
	global_load_dwordx4 v[2:5], v1, s[36:37] sc0 sc1
	global_load_dwordx4 v[6:9], v1, s[8:9] sc0 sc1
	global_load_dwordx4 v[10:13], v1, s[10:11] sc0 sc1
	global_load_dwordx4 v[14:17], v1, s[12:13] sc0 sc1
	global_load_dwordx4 v[18:21], v1, s[14:15] sc0 sc1
	global_load_dwordx4 v[22:25], v1, s[18:19] sc0 sc1
	global_load_dwordx4 v[26:29], v1, s[20:21] sc0 sc1
	global_load_dwordx4 v[30:33], v1, s[84:85] sc0 sc1
	s_nop 4
	global_load_dwordx4 v[98:101], v1, s[66:67] sc0 sc1
	global_load_dwordx4 v[102:105], v1, s[70:71] sc0 sc1
	global_load_dwordx4 v[106:109], v1, s[76:77] sc0 sc1
	global_load_dwordx4 v[110:113], v1, s[82:83] sc0 sc1
	global_load_dwordx4 v[114:117], v1, s[4:5] sc0 sc1
	global_load_dwordx4 v[118:121], v1, s[86:87] sc0 sc1
	global_load_dwordx4 v[122:125], v1, s[90:91] sc0 sc1
	s_waitcnt lgkmcnt(0)
	s_barrier
	s_waitcnt vmcnt(0)
	s_waitcnt vmcnt(0)
	s_waitcnt vmcnt(0)
	v_readlane_b32 s88, v254, 58
	v_readlane_b32 s89, v254, 59
	v_readlane_b32 s90, v254, 60
	v_readlane_b32 s91, v254, 61
	v_readlane_b32 s92, v254, 62
	v_readlane_b32 s93, v254, 63
	v_readlane_b32 s94, v255, 0
	v_readlane_b32 s95, v255, 1
